# adds: in-projection hand-off publishes hierarchically (one L2 write-back per XCD instead of one per workgroup)
# speedup vs baseline: 1.0500x; 1.0042x over previous
; #define PG8_BAR __builtin_amdgcn_s_barrier()
; template <class Epi, class Sched, bool FP8 = false>
; __device__ __forceinline__ void gemm_phase(LAS unsigned char* lds, const int K, const Sched& S, const Epi& E) {
;     ...
;         if constexpr (Sched::HOOK) { if (ui == Sched::HOOK_UNIT) { asm volatile("s_waitcnt vmcnt(0)" ::: "memory"); PG8_BAR; S.publish(); } }
;     __device__ __forceinline__ void publish() const {
;         if (D.G == 256 && threadIdx.x == 0) { __builtin_amdgcn_fence(__ATOMIC_RELEASE, "agent"); asm volatile("s_waitcnt vmcnt(0)" ::: "memory"); (void)__hip_atomic_fetch_add(done, 1u, __ATOMIC_RELAXED, __HIP_MEMORY_SCOPE_AGENT); } }
.LBB0_237:
	s_waitcnt vmcnt(0)
	s_barrier
	s_and_saveexec_b64 s[2:3], s[78:79]
	s_cbranch_execz .LBB0_240
	v_readlane_b32 s34, v246, 21
	v_readlane_b32 s25, v246, 22
	s_nop 3
	s_lshl_b32 s34, s34, 6
	s_add_u32 s34, s34, 0xf000
	s_add_u32 s34, s92, s34
	s_addc_u32 s35, s93, 0
	v_mov_b32_e32 v142, s25
	ds_read_b32 v142, v142
	s_waitcnt lgkmcnt(0)
	v_readfirstlane_b32 s25, v142
	v_mov_b32_e32 v142, 1
	global_atomic_add v142, v143, v142, s[34:35] sc0
	s_waitcnt vmcnt(0)
	v_readfirstlane_b32 s70, v142
	s_add_i32 s70, s70, 1
	s_cmp_lg_u32 s70, s25
	s_cbranch_scc1 .LBB0_240
	buffer_wbl2 sc1
	s_waitcnt vmcnt(0)
	v_mov_b32_e32 v142, s25
	global_atomic_add v143, v142, s[4:5]
